# adds out-proj layer-0 (f32 residual) epilogue prefetch in two batches
# baseline (speedup 1.0000x reference)
.LBB0_754:
	s_mov_b32 s5, s61
	v_mbcnt_lo_u32_b32 v144, -1, 0
	v_mbcnt_hi_u32_b32 v144, -1, v144
	s_lshl_b32 s19, s4, 8
	v_lshl_or_b32 v128, s5, 6, v144
	s_lshl_b32 s5, s24, 8
	v_readfirstlane_b32 s17, v128
	s_lshr_b32 s24, s17, 1
	s_and_b32 s24, s24, 0x60
	s_or_b32 s5, s24, s5
	v_lshrrev_b32_e32 v128, 1, v144
	s_ashr_i32 s4, s4, 3
	v_and_or_b32 v152, v128, 24, s5
	s_mul_hi_i32 s5, s4, 0x6000
	s_mulk_i32 s4, 0x6000
	s_add_u32 s4, s50, s4
	s_addc_u32 s5, s51, s5
	v_ashrrev_i32_e32 v153, 31, v152
	v_lshl_add_u64 v[132:133], v[152:153], 2, s[4:5]
	global_load_dwordx4 v[136:139], v[132:133], off offset:16
	global_load_dwordx4 v[140:143], v[132:133], off
	global_load_dwordx4 v[128:131], v[132:133], off offset:528
	s_nop 0
	global_load_dwordx4 v[132:135], v[132:133], off offset:512
	s_ashr_i32 s4, s17, 2
	s_andn2_b32 s4, s4, 63
	v_lshlrev_b32_e32 v145, 1, v144
	v_and_b32_e32 v145, 24, v145
	v_and_b32_e32 v144, 3, v144
	s_add_i32 s4, s4, s19
	v_or3_b32 v154, s4, v144, v145
	v_ashrrev_i32_e32 v155, 31, v154
	v_lshlrev_b64 v[144:145], 10, v[154:155]
	v_lshl_add_u64 v[156:157], v[144:145], 0, v[152:153]
	v_cndmask_b32_e64 v144, 0, 1, s[14:15]
	v_cmp_ne_u32_e64 s[4:5], 1, v144
	s_andn2_b64 vcc, exec, s[14:15]
	v_lshl_add_u64 v[158:159], v[156:157], 2, s[6:7]
	s_cbranch_vccnz .LBB0_805
	global_load_dwordx4 v[166:169], v[158:159], off offset:16
	global_load_dwordx4 v[170:173], v[158:159], off
	global_load_dwordx4 v[174:177], v[158:159], off offset:528
	global_load_dwordx4 v[178:181], v[158:159], off offset:512
	s_mov_b64 s[78:79], 0x4000
	v_lshl_add_u64 v[250:251], v[158:159], 0, s[78:79]
	global_load_dwordx4 v[186:189], v[250:251], off offset:16
	global_load_dwordx4 v[190:193], v[250:251], off
	global_load_dwordx4 v[194:197], v[250:251], off offset:528
	global_load_dwordx4 v[198:201], v[250:251], off offset:512
	s_mov_b64 s[78:79], 0x20000
	v_lshl_add_u64 v[248:249], v[158:159], 0, s[78:79]
	global_load_dwordx4 v[202:205], v[248:249], off offset:16
	global_load_dwordx4 v[206:209], v[248:249], off
	global_load_dwordx4 v[210:213], v[248:249], off offset:528
	global_load_dwordx4 v[214:217], v[248:249], off offset:512
	s_mov_b64 s[78:79], 0x24000
	v_lshl_add_u64 v[250:251], v[158:159], 0, s[78:79]
	global_load_dwordx4 v[228:231], v[250:251], off offset:16
	global_load_dwordx4 v[232:235], v[250:251], off
	global_load_dwordx4 v[236:239], v[250:251], off offset:528
	global_load_dwordx4 v[244:247], v[250:251], off offset:512
	s_waitcnt vmcnt(14)
	v_mov_b64_e32 v[148:149], v[166:167]
	v_mov_b64_e32 v[150:151], v[168:169]
	v_mov_b64_e32 v[144:145], v[170:171]
	v_mov_b64_e32 v[146:147], v[172:173]
	v_lshl_add_u64 v[156:157], v[156:157], 1, s[10:11]
	v_mov_b32_e32 v218, v183
	s_cbranch_execnz .LBB0_757

.LBB0_757:
	s_mov_b32 s24, 0x3b000000
	v_pk_mul_f32 v[140:141], v[140:141], s[24:25] op_sel_hi:[1,0]
	v_pk_mul_f32 v[138:139], v[138:139], s[24:25] op_sel_hi:[1,0]
	v_pk_mul_f32 v[136:137], v[136:137], s[24:25] op_sel_hi:[1,0]
	v_pk_mul_f32 v[142:143], v[142:143], s[24:25] op_sel_hi:[1,0]
	v_pk_fma_f32 v[124:125], v[124:125], v[140:141], v[144:145]
	v_pk_fma_f32 v[144:145], v[122:123], v[138:139], v[150:151]
	v_pk_fma_f32 v[122:123], v[120:121], v[136:137], v[148:149]
	s_and_b64 vcc, exec, s[4:5]
	v_pk_fma_f32 v[126:127], v[126:127], v[142:143], v[146:147]
	v_cvt_pk_bf16_f32 v120, v124, v125
	s_nop 0
	v_cvt_pk_bf16_f32 v121, v126, v127
	v_cvt_pk_bf16_f32 v122, v122, v123
	v_cvt_pk_bf16_f32 v123, v144, v145
	global_store_dwordx4 v[156:157], v[120:123], off
	s_cbranch_vccnz .LBB0_806
	s_waitcnt vmcnt(13)
	v_mov_b64_e32 v[124:125], v[174:175]
	v_mov_b64_e32 v[126:127], v[176:177]
	v_mov_b64_e32 v[120:121], v[178:179]
	v_mov_b64_e32 v[122:123], v[180:181]
	s_cbranch_execnz .LBB0_760

.LBB0_760:
	s_mov_b32 s24, 0x3b000000
	v_pk_mul_f32 v[132:133], v[132:133], s[24:25] op_sel_hi:[1,0]
	v_pk_mul_f32 v[130:131], v[130:131], s[24:25] op_sel_hi:[1,0]
	v_pk_mul_f32 v[128:129], v[128:129], s[24:25] op_sel_hi:[1,0]
	v_pk_mul_f32 v[134:135], v[134:135], s[24:25] op_sel_hi:[1,0]
	v_pk_fma_f32 v[116:117], v[116:117], v[132:133], v[120:121]
	v_pk_fma_f32 v[120:121], v[114:115], v[130:131], v[126:127]
	v_pk_fma_f32 v[114:115], v[112:113], v[128:129], v[124:125]
	v_cvt_pk_bf16_f32 v112, v116, v117
	v_pk_fma_f32 v[118:119], v[118:119], v[134:135], v[122:123]
	s_and_b64 vcc, exec, s[4:5]
	v_cvt_pk_bf16_f32 v113, v118, v119
	v_cvt_pk_bf16_f32 v114, v114, v115
	v_cvt_pk_bf16_f32 v115, v120, v121
	global_store_dwordx4 v[156:157], v[112:115], off offset:256
	s_nop 1
	v_or_b32_e32 v112, 4, v154
	v_ashrrev_i32_e32 v113, 31, v112
	v_lshlrev_b64 v[112:113], 10, v[112:113]
	v_lshl_add_u64 v[120:121], v[112:113], 0, v[152:153]
	v_lshl_add_u64 v[122:123], v[120:121], 2, s[6:7]
	s_cbranch_vccnz .LBB0_807
	s_waitcnt vmcnt(12)
	v_mov_b64_e32 v[116:117], v[186:187]
	v_mov_b64_e32 v[118:119], v[188:189]
	v_mov_b64_e32 v[112:113], v[190:191]
	v_mov_b64_e32 v[114:115], v[192:193]
	v_lshl_add_u64 v[120:121], v[120:121], 1, s[10:11]
	s_cbranch_execnz .LBB0_763

.LBB0_763:
	v_pk_fma_f32 v[108:109], v[108:109], v[140:141], v[112:113]
	v_pk_fma_f32 v[112:113], v[106:107], v[138:139], v[118:119]
	v_pk_fma_f32 v[106:107], v[104:105], v[136:137], v[116:117]
	s_and_b64 vcc, exec, s[4:5]
	v_pk_fma_f32 v[110:111], v[110:111], v[142:143], v[114:115]
	v_cvt_pk_bf16_f32 v104, v108, v109
	s_nop 0
	v_cvt_pk_bf16_f32 v105, v110, v111
	v_cvt_pk_bf16_f32 v106, v106, v107
	v_cvt_pk_bf16_f32 v107, v112, v113
	global_store_dwordx4 v[120:121], v[104:107], off
	s_cbranch_vccnz .LBB0_808
	s_waitcnt vmcnt(11)
	v_mov_b64_e32 v[108:109], v[194:195]
	v_mov_b64_e32 v[110:111], v[196:197]
	v_mov_b64_e32 v[104:105], v[198:199]
	v_mov_b64_e32 v[106:107], v[200:201]
	s_cbranch_execnz .LBB0_766

.LBB0_766:
	v_pk_fma_f32 v[100:101], v[100:101], v[132:133], v[104:105]
	v_pk_fma_f32 v[104:105], v[98:99], v[130:131], v[110:111]
	v_pk_fma_f32 v[98:99], v[96:97], v[128:129], v[108:109]
	v_cvt_pk_bf16_f32 v96, v100, v101
	v_pk_fma_f32 v[102:103], v[102:103], v[134:135], v[106:107]
	s_and_b64 vcc, exec, s[4:5]
	v_cvt_pk_bf16_f32 v97, v102, v103
	v_cvt_pk_bf16_f32 v98, v98, v99
	v_cvt_pk_bf16_f32 v99, v104, v105
	global_store_dwordx4 v[120:121], v[96:99], off offset:256
	s_nop 1
	v_or_b32_e32 v96, 32, v154
	v_ashrrev_i32_e32 v97, 31, v96
	v_lshlrev_b64 v[96:97], 10, v[96:97]
	v_lshl_add_u64 v[104:105], v[96:97], 0, v[152:153]
	v_lshl_add_u64 v[106:107], v[104:105], 2, s[6:7]
	s_cbranch_vccnz .LBB0_809
	s_waitcnt vmcnt(10)
	v_mov_b64_e32 v[100:101], v[202:203]
	v_mov_b64_e32 v[102:103], v[204:205]
	v_mov_b64_e32 v[96:97], v[206:207]
	v_mov_b64_e32 v[98:99], v[208:209]
	v_lshl_add_u64 v[104:105], v[104:105], 1, s[10:11]
	s_cbranch_execnz .LBB0_769

.LBB0_769:
	v_pk_fma_f32 v[92:93], v[92:93], v[140:141], v[96:97]
	v_pk_fma_f32 v[96:97], v[90:91], v[138:139], v[102:103]
	v_pk_fma_f32 v[90:91], v[88:89], v[136:137], v[100:101]
	s_and_b64 vcc, exec, s[4:5]
	v_pk_fma_f32 v[94:95], v[94:95], v[142:143], v[98:99]
	v_cvt_pk_bf16_f32 v88, v92, v93
	s_nop 0
	v_cvt_pk_bf16_f32 v89, v94, v95
	v_cvt_pk_bf16_f32 v90, v90, v91
	v_cvt_pk_bf16_f32 v91, v96, v97
	global_store_dwordx4 v[104:105], v[88:91], off
	s_cbranch_vccnz .LBB0_810
	s_waitcnt vmcnt(9)
	v_mov_b64_e32 v[92:93], v[210:211]
	v_mov_b64_e32 v[94:95], v[212:213]
	v_mov_b64_e32 v[88:89], v[214:215]
	v_mov_b64_e32 v[90:91], v[216:217]
	s_cbranch_execnz .LBB0_772

.LBB0_772:
	v_pk_fma_f32 v[84:85], v[84:85], v[132:133], v[88:89]
	v_pk_fma_f32 v[88:89], v[82:83], v[130:131], v[94:95]
	v_pk_fma_f32 v[82:83], v[80:81], v[128:129], v[92:93]
	v_cvt_pk_bf16_f32 v80, v84, v85
	v_pk_fma_f32 v[86:87], v[86:87], v[134:135], v[90:91]
	s_and_b64 vcc, exec, s[4:5]
	v_cvt_pk_bf16_f32 v81, v86, v87
	v_cvt_pk_bf16_f32 v82, v82, v83
	v_cvt_pk_bf16_f32 v83, v88, v89
	global_store_dwordx4 v[104:105], v[80:83], off offset:256
	s_nop 1
	v_or_b32_e32 v80, 36, v154
	v_ashrrev_i32_e32 v81, 31, v80
	v_lshlrev_b64 v[80:81], 10, v[80:81]
	v_lshl_add_u64 v[88:89], v[80:81], 0, v[152:153]
	v_lshl_add_u64 v[90:91], v[88:89], 2, s[6:7]
	s_cbranch_vccnz .LBB0_811
	s_waitcnt vmcnt(8)
	v_mov_b64_e32 v[84:85], v[228:229]
	v_mov_b64_e32 v[86:87], v[230:231]
	v_mov_b64_e32 v[80:81], v[232:233]
	v_mov_b64_e32 v[82:83], v[234:235]
	v_lshl_add_u64 v[88:89], v[88:89], 1, s[10:11]
	s_cbranch_execnz .LBB0_775

.LBB0_775:
	v_pk_fma_f32 v[76:77], v[76:77], v[140:141], v[80:81]
	v_pk_fma_f32 v[80:81], v[74:75], v[138:139], v[86:87]
	v_pk_fma_f32 v[74:75], v[72:73], v[136:137], v[84:85]
	s_and_b64 vcc, exec, s[4:5]
	v_pk_fma_f32 v[78:79], v[78:79], v[142:143], v[82:83]
	v_cvt_pk_bf16_f32 v72, v76, v77
	s_nop 0
	v_cvt_pk_bf16_f32 v73, v78, v79
	v_cvt_pk_bf16_f32 v74, v74, v75
	v_cvt_pk_bf16_f32 v75, v80, v81
	global_store_dwordx4 v[88:89], v[72:75], off
	s_cbranch_vccnz .LBB0_812
	s_waitcnt vmcnt(7)
	v_mov_b64_e32 v[76:77], v[236:237]
	v_mov_b64_e32 v[78:79], v[238:239]
	v_mov_b64_e32 v[72:73], v[244:245]
	v_mov_b64_e32 v[74:75], v[246:247]
	s_cbranch_execnz .LBB0_778

.LBB0_778:
	v_pk_fma_f32 v[68:69], v[68:69], v[132:133], v[72:73]
	v_pk_fma_f32 v[72:73], v[66:67], v[130:131], v[78:79]
	v_pk_fma_f32 v[66:67], v[64:65], v[128:129], v[76:77]
	v_pk_fma_f32 v[70:71], v[70:71], v[134:135], v[74:75]
	v_cvt_pk_bf16_f32 v64, v68, v69
	s_and_b64 vcc, exec, s[4:5]
	v_cvt_pk_bf16_f32 v65, v70, v71
	v_cvt_pk_bf16_f32 v66, v66, v67
	v_cvt_pk_bf16_f32 v67, v72, v73
	v_add_u32_e32 v72, 0x80, v154
	v_ashrrev_i32_e32 v73, 31, v72
	global_store_dwordx4 v[88:89], v[64:67], off offset:256
	s_nop 1
	v_lshlrev_b64 v[64:65], 10, v[72:73]
	v_lshl_add_u64 v[74:75], v[64:65], 0, v[152:153]
	v_lshl_add_u64 v[76:77], v[74:75], 2, s[6:7]
	s_cbranch_vccnz .LBB0_813
	s_mov_b64 s[78:79], 0x80000
	v_lshl_add_u64 v[248:249], v[158:159], 0, s[78:79]
	global_load_dwordx4 v[166:169], v[248:249], off offset:16
	global_load_dwordx4 v[170:173], v[248:249], off
	global_load_dwordx4 v[174:177], v[248:249], off offset:528
	global_load_dwordx4 v[178:181], v[248:249], off offset:512
	s_mov_b64 s[78:79], 0x84000
	v_lshl_add_u64 v[250:251], v[158:159], 0, s[78:79]
	global_load_dwordx4 v[186:189], v[250:251], off offset:16
	global_load_dwordx4 v[190:193], v[250:251], off
	global_load_dwordx4 v[194:197], v[250:251], off offset:528
	global_load_dwordx4 v[198:201], v[250:251], off offset:512
	s_mov_b64 s[78:79], 0xa0000
	v_lshl_add_u64 v[248:249], v[158:159], 0, s[78:79]
	global_load_dwordx4 v[202:205], v[248:249], off offset:16
	global_load_dwordx4 v[206:209], v[248:249], off
	global_load_dwordx4 v[210:213], v[248:249], off offset:528
	global_load_dwordx4 v[214:217], v[248:249], off offset:512
	s_mov_b64 s[78:79], 0xa4000
	v_lshl_add_u64 v[250:251], v[158:159], 0, s[78:79]
	global_load_dwordx4 v[228:231], v[250:251], off offset:16
	global_load_dwordx4 v[232:235], v[250:251], off
	global_load_dwordx4 v[236:239], v[250:251], off offset:528
	global_load_dwordx4 v[244:247], v[250:251], off offset:512
	s_waitcnt vmcnt(14)
	v_mov_b64_e32 v[68:69], v[166:167]
	v_mov_b64_e32 v[70:71], v[168:169]
	v_mov_b64_e32 v[64:65], v[170:171]
	v_mov_b64_e32 v[66:67], v[172:173]
	v_lshl_add_u64 v[74:75], v[74:75], 1, s[10:11]
	s_cbranch_execnz .LBB0_781

.LBB0_781:
	v_pk_fma_f32 v[60:61], v[60:61], v[140:141], v[64:65]
	v_pk_fma_f32 v[64:65], v[58:59], v[138:139], v[70:71]
	v_pk_fma_f32 v[58:59], v[56:57], v[136:137], v[68:69]
	s_and_b64 vcc, exec, s[4:5]
	v_pk_fma_f32 v[62:63], v[62:63], v[142:143], v[66:67]
	v_cvt_pk_bf16_f32 v56, v60, v61
	s_nop 0
	v_cvt_pk_bf16_f32 v57, v62, v63
	v_cvt_pk_bf16_f32 v58, v58, v59
	v_cvt_pk_bf16_f32 v59, v64, v65
	global_store_dwordx4 v[74:75], v[56:59], off
	s_cbranch_vccnz .LBB0_814
	s_waitcnt vmcnt(13)
	v_mov_b64_e32 v[60:61], v[174:175]
	v_mov_b64_e32 v[62:63], v[176:177]
	v_mov_b64_e32 v[56:57], v[178:179]
	v_mov_b64_e32 v[58:59], v[180:181]
	s_cbranch_execnz .LBB0_784

.LBB0_784:
	v_pk_fma_f32 v[52:53], v[52:53], v[132:133], v[56:57]
	v_pk_fma_f32 v[56:57], v[50:51], v[130:131], v[62:63]
	v_pk_fma_f32 v[50:51], v[48:49], v[128:129], v[60:61]
	v_cvt_pk_bf16_f32 v48, v52, v53
	v_pk_fma_f32 v[54:55], v[54:55], v[134:135], v[58:59]
	s_and_b64 vcc, exec, s[4:5]
	v_cvt_pk_bf16_f32 v49, v54, v55
	v_cvt_pk_bf16_f32 v50, v50, v51
	v_cvt_pk_bf16_f32 v51, v56, v57
	global_store_dwordx4 v[74:75], v[48:51], off offset:256
	s_nop 1
	v_or_b32_e32 v48, 4, v72
	v_ashrrev_i32_e32 v49, 31, v48
	v_lshlrev_b64 v[48:49], 10, v[48:49]
	v_lshl_add_u64 v[56:57], v[48:49], 0, v[152:153]
	v_lshl_add_u64 v[58:59], v[56:57], 2, s[6:7]
	s_cbranch_vccnz .LBB0_815
	s_waitcnt vmcnt(12)
	v_mov_b64_e32 v[52:53], v[186:187]
	v_mov_b64_e32 v[54:55], v[188:189]
	v_mov_b64_e32 v[48:49], v[190:191]
	v_mov_b64_e32 v[50:51], v[192:193]
	v_lshl_add_u64 v[56:57], v[56:57], 1, s[10:11]
	s_cbranch_execnz .LBB0_787

.LBB0_787:
	v_pk_fma_f32 v[44:45], v[44:45], v[140:141], v[48:49]
	v_pk_fma_f32 v[48:49], v[42:43], v[138:139], v[54:55]
	v_pk_fma_f32 v[42:43], v[40:41], v[136:137], v[52:53]
	s_and_b64 vcc, exec, s[4:5]
	v_pk_fma_f32 v[46:47], v[46:47], v[142:143], v[50:51]
	v_cvt_pk_bf16_f32 v40, v44, v45
	s_nop 0
	v_cvt_pk_bf16_f32 v41, v46, v47
	v_cvt_pk_bf16_f32 v42, v42, v43
	v_cvt_pk_bf16_f32 v43, v48, v49
	global_store_dwordx4 v[56:57], v[40:43], off
	s_cbranch_vccnz .LBB0_816
	s_waitcnt vmcnt(11)
	v_mov_b64_e32 v[44:45], v[194:195]
	v_mov_b64_e32 v[46:47], v[196:197]
	v_mov_b64_e32 v[40:41], v[198:199]
	v_mov_b64_e32 v[42:43], v[200:201]
	s_cbranch_execnz .LBB0_790

.LBB0_790:
	v_pk_fma_f32 v[36:37], v[36:37], v[132:133], v[40:41]
	v_pk_fma_f32 v[40:41], v[34:35], v[130:131], v[46:47]
	v_pk_fma_f32 v[34:35], v[32:33], v[128:129], v[44:45]
	v_cvt_pk_bf16_f32 v32, v36, v37
	v_pk_fma_f32 v[38:39], v[38:39], v[134:135], v[42:43]
	s_and_b64 vcc, exec, s[4:5]
	v_cvt_pk_bf16_f32 v33, v38, v39
	v_cvt_pk_bf16_f32 v34, v34, v35
	v_cvt_pk_bf16_f32 v35, v40, v41
	global_store_dwordx4 v[56:57], v[32:35], off offset:256
	s_nop 1
	v_or_b32_e32 v32, 32, v72
	v_ashrrev_i32_e32 v33, 31, v32
	v_lshlrev_b64 v[32:33], 10, v[32:33]
	v_lshl_add_u64 v[40:41], v[32:33], 0, v[152:153]
	v_lshl_add_u64 v[42:43], v[40:41], 2, s[6:7]
	s_cbranch_vccnz .LBB0_817
	s_waitcnt vmcnt(10)
	v_mov_b64_e32 v[36:37], v[202:203]
	v_mov_b64_e32 v[38:39], v[204:205]
	v_mov_b64_e32 v[32:33], v[206:207]
	v_mov_b64_e32 v[34:35], v[208:209]
	v_lshl_add_u64 v[40:41], v[40:41], 1, s[10:11]
	s_cbranch_execnz .LBB0_793

.LBB0_793:
	v_pk_fma_f32 v[28:29], v[28:29], v[140:141], v[32:33]
	v_pk_fma_f32 v[32:33], v[26:27], v[138:139], v[38:39]
	v_pk_fma_f32 v[26:27], v[24:25], v[136:137], v[36:37]
	s_and_b64 vcc, exec, s[4:5]
	v_pk_fma_f32 v[30:31], v[30:31], v[142:143], v[34:35]
	v_cvt_pk_bf16_f32 v24, v28, v29
	s_nop 0
	v_cvt_pk_bf16_f32 v25, v30, v31
	v_cvt_pk_bf16_f32 v26, v26, v27
	v_cvt_pk_bf16_f32 v27, v32, v33
	global_store_dwordx4 v[40:41], v[24:27], off
	s_cbranch_vccnz .LBB0_818
	s_waitcnt vmcnt(9)
	v_mov_b64_e32 v[28:29], v[210:211]
	v_mov_b64_e32 v[30:31], v[212:213]
	v_mov_b64_e32 v[24:25], v[214:215]
	v_mov_b64_e32 v[26:27], v[216:217]
	s_cbranch_execnz .LBB0_796

.LBB0_796:
	v_pk_fma_f32 v[20:21], v[20:21], v[132:133], v[24:25]
	v_pk_fma_f32 v[24:25], v[18:19], v[130:131], v[30:31]
	v_pk_fma_f32 v[18:19], v[16:17], v[128:129], v[28:29]
	v_cvt_pk_bf16_f32 v16, v20, v21
	v_pk_fma_f32 v[22:23], v[22:23], v[134:135], v[26:27]
	s_and_b64 vcc, exec, s[4:5]
	v_cvt_pk_bf16_f32 v17, v22, v23
	v_cvt_pk_bf16_f32 v18, v18, v19
	v_cvt_pk_bf16_f32 v19, v24, v25
	global_store_dwordx4 v[40:41], v[16:19], off offset:256
	s_nop 1
	v_or_b32_e32 v16, 36, v72
	v_ashrrev_i32_e32 v17, 31, v16
	v_lshlrev_b64 v[16:17], 10, v[16:17]
	v_lshl_add_u64 v[24:25], v[16:17], 0, v[152:153]
	v_lshl_add_u64 v[26:27], v[24:25], 2, s[6:7]
	s_cbranch_vccnz .LBB0_819
	s_waitcnt vmcnt(8)
	v_mov_b64_e32 v[20:21], v[228:229]
	v_mov_b64_e32 v[22:23], v[230:231]
	v_mov_b64_e32 v[16:17], v[232:233]
	v_mov_b64_e32 v[18:19], v[234:235]
	v_lshl_add_u64 v[24:25], v[24:25], 1, s[10:11]
	s_cbranch_execnz .LBB0_799

.LBB0_799:
	v_pk_fma_f32 v[12:13], v[12:13], v[140:141], v[16:17]
	v_pk_fma_f32 v[16:17], v[10:11], v[138:139], v[22:23]
	v_pk_fma_f32 v[10:11], v[8:9], v[136:137], v[20:21]
	s_and_b64 vcc, exec, s[4:5]
	v_pk_fma_f32 v[14:15], v[14:15], v[142:143], v[18:19]
	v_cvt_pk_bf16_f32 v8, v12, v13
	s_nop 0
	v_cvt_pk_bf16_f32 v9, v14, v15
	v_cvt_pk_bf16_f32 v10, v10, v11
	v_cvt_pk_bf16_f32 v11, v16, v17
	global_store_dwordx4 v[24:25], v[8:11], off
	s_cbranch_vccnz .LBB0_820
	s_waitcnt vmcnt(7)
	v_mov_b64_e32 v[12:13], v[236:237]
	v_mov_b64_e32 v[14:15], v[238:239]
	v_mov_b64_e32 v[8:9], v[244:245]
	v_mov_b64_e32 v[10:11], v[246:247]
	s_cbranch_execnz .LBB0_802
